# speedup vs baseline: 1.0038x; 1.0038x over previous
.LBB0_78:
	s_sleep 20
	s_load_dwordx2 s[0:1], s[0:1], 0x28
	v_lshlrev_b32_e32 v2, 9, v0
	v_and_b32_e32 v13, 3, v0
	v_and_b32_e32 v2, 0x7800, v2
	v_mov_b32_e32 v3, 0
	v_lshl_or_b32 v12, s36, 2, v13
	s_waitcnt lgkmcnt(0)
	s_mov_b64 s[44:45], s[0:1]
	v_and_b32_e32 v164, 15, v0
	v_lshlrev_b32_e32 v164, 2, v164
	v_add_u32_e32 v164, 0x14a80, v164
	v_mov_b32_e32 v165, 0
	ds_write_b32 v164, v165
	v_lshl_add_u64 v[4:5], s[0:1], 0, v[2:3]
	s_lshl_b32 s0, s33, 7
	v_lshl_or_b32 v2, v12, 3, s0
	v_lshl_add_u64 v[10:11], v[4:5], 0, v[2:3]
	v_and_b32_e32 v160, 15, v0
	v_bfe_u32 v161, v0, 4, 2
	s_and_b32 s46, s36, 1
	s_lshl_b32 s46, s46, 5
	v_lshl_add_u32 v162, v161, 3, s46
	v_lshlrev_b32_e32 v162, 7, v162
	s_lshl_b32 s47, s33, 5
	s_lshr_b32 s46, s36, 1
	s_add_i32 s47, s47, s46
	v_lshl_add_u32 v163, v160, 1, s47
	v_add_lshl_u32 v162, v162, v163, 2
	global_load_dword v152, v162, s[44:45]
	global_load_dword v153, v162, s[44:45] offset:512
	global_load_dword v154, v162, s[44:45] offset:1024
	global_load_dword v155, v162, s[44:45] offset:1536
	global_load_dword v156, v162, s[44:45] offset:2048
	global_load_dword v157, v162, s[44:45] offset:2560
	global_load_dword v158, v162, s[44:45] offset:3072
	global_load_dword v159, v162, s[44:45] offset:3584
	s_bfe_u32 s5, s2, 0x30002
	s_mov_b32 s4, 2
	s_cmp_gt_u32 s5, 3
	v_lshlrev_b32_e32 v10, 2, v0
	s_cbranch_scc0 .LBB0_80
	v_and_b32_e32 v11, 16, v10
	v_lshl_or_b32 v14, s5, 5, v11
	s_cbranch_execz .LBB0_81
	s_branch .LBB0_82
